# attn stores with sc0 nt cache policy instead of nt
# speedup vs baseline: 1.0098x; 1.0098x over previous
.Lkb_skip:
	v_div_scale_f32 v1, s[64:65], v253, v253, v252
	v_rcp_f32_e32 v2, v1
	s_nop 0
	v_fma_f32 v0, -v1, v2, 1.0
	v_fmac_f32_e32 v2, v0, v2
	v_div_scale_f32 v0, vcc, v252, v253, v252
	v_mul_f32_e32 v3, v0, v2
	v_fma_f32 v248, -v1, v3, v0
	v_fmac_f32_e32 v3, v248, v2
	v_fma_f32 v0, -v1, v3, v0
	v_div_fmas_f32 v0, v0, v2, v3
	v_div_fixup_f32 v1, v0, v253, v252
	v_mul_f32_e32 v0, s18, v1
	v_mov_b32_e32 v2, s26
	v_mov_b32_e32 v3, s23
	v_cmp_eq_u32_e64 s[64:65], 0, v233
	v_cmp_eq_u32_e64 s[66:67], 1, v233
	v_cmp_eq_u32_e64 s[68:69], 2, v233
	v_cmp_eq_u32_e64 s[70:71], 3, v233
	v_cndmask_b32_e64 v248, v2, v3, s[64:65]
	v_cndmask_b32_e64 v249, v2, v3, s[66:67]
	v_cndmask_b32_e64 v250, v2, v3, s[68:69]
	v_cndmask_b32_e64 v251, v2, v3, s[70:71]
	v_mul_f32_e32 v248, v1, v248
	v_mul_f32_e32 v249, v1, v249
	v_mul_f32_e32 v250, v1, v250
	v_mul_f32_e32 v251, v1, v251
	v_cndmask_b32_e64 v248, v0, v248, s[2:3]
	v_cndmask_b32_e64 v249, v0, v249, s[2:3]
	v_cndmask_b32_e64 v250, v0, v250, s[2:3]
	v_cndmask_b32_e64 v251, v0, v251, s[2:3]
	v_mul_f32_e32 v248, v248, v208
	v_mul_f32_e32 v249, v249, v209
	v_mul_f32_e32 v250, v250, v204
	v_mul_f32_e32 v251, v251, v205
	ds_write_b128 v238, v[248:251]
	v_cmp_eq_u32_e64 s[64:65], 4, v233
	v_cmp_eq_u32_e64 s[66:67], 5, v233
	v_cmp_eq_u32_e64 s[68:69], 6, v233
	v_cmp_eq_u32_e64 s[70:71], 7, v233
	v_cndmask_b32_e64 v248, v2, v3, s[64:65]
	v_cndmask_b32_e64 v249, v2, v3, s[66:67]
	v_cndmask_b32_e64 v250, v2, v3, s[68:69]
	v_cndmask_b32_e64 v251, v2, v3, s[70:71]
	v_mul_f32_e32 v248, v1, v248
	v_mul_f32_e32 v249, v1, v249
	v_mul_f32_e32 v250, v1, v250
	v_mul_f32_e32 v251, v1, v251
	v_cndmask_b32_e64 v248, v0, v248, s[2:3]
	v_cndmask_b32_e64 v249, v0, v249, s[2:3]
	v_cndmask_b32_e64 v250, v0, v250, s[2:3]
	v_cndmask_b32_e64 v251, v0, v251, s[2:3]
	v_mul_f32_e32 v248, v248, v182
	v_mul_f32_e32 v249, v249, v183
	v_mul_f32_e32 v250, v250, v178
	v_mul_f32_e32 v251, v251, v179
	ds_write_b128 v238, v[248:251] offset:32
	v_cmp_eq_u32_e64 s[64:65], 8, v233
	v_cmp_eq_u32_e64 s[66:67], 9, v233
	v_cmp_eq_u32_e64 s[68:69], 10, v233
	v_cmp_eq_u32_e64 s[70:71], 11, v233
	v_cndmask_b32_e64 v248, v2, v3, s[64:65]
	v_cndmask_b32_e64 v249, v2, v3, s[66:67]
	v_cndmask_b32_e64 v250, v2, v3, s[68:69]
	v_cndmask_b32_e64 v251, v2, v3, s[70:71]
	v_mul_f32_e32 v248, v1, v248
	v_mul_f32_e32 v249, v1, v249
	v_mul_f32_e32 v250, v1, v250
	v_mul_f32_e32 v251, v1, v251
	v_cndmask_b32_e64 v248, v0, v248, s[2:3]
	v_cndmask_b32_e64 v249, v0, v249, s[2:3]
	v_cndmask_b32_e64 v250, v0, v250, s[2:3]
	v_cndmask_b32_e64 v251, v0, v251, s[2:3]
	v_mul_f32_e32 v248, v248, v166
	v_mul_f32_e32 v249, v249, v167
	v_mul_f32_e32 v250, v250, v118
	v_mul_f32_e32 v251, v251, v119
	ds_write_b128 v238, v[248:251] offset:64
	v_cmp_eq_u32_e64 s[64:65], 12, v233
	v_cmp_eq_u32_e64 s[66:67], 13, v233
	v_cmp_eq_u32_e64 s[68:69], 14, v233
	v_cmp_eq_u32_e64 s[70:71], 15, v233
	v_cndmask_b32_e64 v248, v2, v3, s[64:65]
	v_cndmask_b32_e64 v249, v2, v3, s[66:67]
	v_cndmask_b32_e64 v250, v2, v3, s[68:69]
	v_cndmask_b32_e64 v251, v2, v3, s[70:71]
	v_mul_f32_e32 v248, v1, v248
	v_mul_f32_e32 v249, v1, v249
	v_mul_f32_e32 v250, v1, v250
	v_mul_f32_e32 v251, v1, v251
	v_cndmask_b32_e64 v248, v0, v248, s[2:3]
	v_cndmask_b32_e64 v249, v0, v249, s[2:3]
	v_cndmask_b32_e64 v250, v0, v250, s[2:3]
	v_cndmask_b32_e64 v251, v0, v251, s[2:3]
	v_mul_f32_e32 v248, v248, v116
	v_mul_f32_e32 v249, v249, v117
	v_mul_f32_e32 v250, v250, v114
	v_mul_f32_e32 v251, v251, v115
	ds_write_b128 v238, v[248:251] offset:96
	v_pk_mul_f32 v[248:249], v[0:1], v[112:113] op_sel_hi:[0,1]
	v_pk_mul_f32 v[250:251], v[0:1], v[98:99] op_sel_hi:[0,1]
	ds_write_b128 v238, v[248:251] offset:128
	v_pk_mul_f32 v[248:249], v[0:1], v[100:101] op_sel_hi:[0,1]
	v_pk_mul_f32 v[250:251], v[0:1], v[120:121] op_sel_hi:[0,1]
	ds_write_b128 v238, v[248:251] offset:160
	v_pk_mul_f32 v[248:249], v[0:1], v[102:103] op_sel_hi:[0,1]
	v_pk_mul_f32 v[250:251], v[0:1], v[122:123] op_sel_hi:[0,1]
	ds_write_b128 v238, v[248:251] offset:192
	v_pk_mul_f32 v[248:249], v[0:1], v[124:125] op_sel_hi:[0,1]
	v_pk_mul_f32 v[250:251], v[0:1], v[180:181] op_sel_hi:[0,1]
	ds_write_b128 v238, v[248:251] offset:224
	s_lshl_b32 s56, s56, 11
	s_add_i32 s56, s56, s25
	v_or_b32_e32 v252, s56, v239
	v_add_lshl_u32 v253, v241, s55, 7
	v_lshl_or_b32 v1, v252, 13, v240
	v_and_or_b32 v2, v253, s54, v1
	ds_read_b128 v[248:251], v246
	ds_read_b128 v[160:163], v246 offset:1088
	s_waitcnt lgkmcnt(1)
	global_store_dwordx4 v2, v[248:251], s[10:11] sc0 nt
	s_nop 0
	ds_read_b128 v[248:251], v246 offset:2176
	v_or_b32_e32 v3, 0x8000, v2
	s_waitcnt lgkmcnt(1)
	global_store_dwordx4 v3, v[160:163], s[10:11] sc0 nt
	s_nop 0
	ds_read_b128 v[160:163], v246 offset:3264
	v_or_b32_e32 v252, 0x10000, v2
	s_waitcnt lgkmcnt(1)
	global_store_dwordx4 v252, v[248:251], s[10:11] sc0 nt
	s_nop 0
	ds_read_b128 v[248:251], v246 offset:4352
	v_or_b32_e32 v3, 0x18000, v2
	s_waitcnt lgkmcnt(1)
	global_store_dwordx4 v3, v[160:163], s[10:11] sc0 nt
	s_nop 0
	ds_read_b128 v[160:163], v246 offset:5440
	v_or_b32_e32 v252, 0x20000, v2
	s_waitcnt lgkmcnt(1)
	global_store_dwordx4 v252, v[248:251], s[10:11] sc0 nt
	s_nop 0
	ds_read_b128 v[248:251], v246 offset:6528
	v_or_b32_e32 v3, 0x28000, v2
	s_waitcnt lgkmcnt(1)
	global_store_dwordx4 v3, v[160:163], s[10:11] sc0 nt
	s_nop 0
	ds_read_b128 v[160:163], v246 offset:7616
	v_or_b32_e32 v252, 0x30000, v2
	s_waitcnt lgkmcnt(1)
	global_store_dwordx4 v252, v[248:251], s[10:11] sc0 nt
	v_or_b32_e32 v3, 0x38000, v2
	s_waitcnt lgkmcnt(0)
	global_store_dwordx4 v3, v[160:163], s[10:11] sc0 nt
	v_pk_mul_f32 v[248:249], v[0:1], v[80:81] op_sel_hi:[0,1]
	v_pk_mul_f32 v[250:251], v[0:1], v[82:83] op_sel_hi:[0,1]
	ds_write_b128 v238, v[248:251]
	v_pk_mul_f32 v[248:249], v[0:1], v[84:85] op_sel_hi:[0,1]
	v_pk_mul_f32 v[250:251], v[0:1], v[96:97] op_sel_hi:[0,1]
	ds_write_b128 v238, v[248:251] offset:32
	v_pk_mul_f32 v[248:249], v[0:1], v[86:87] op_sel_hi:[0,1]
	v_pk_mul_f32 v[250:251], v[0:1], v[88:89] op_sel_hi:[0,1]
	ds_write_b128 v238, v[248:251] offset:64
	v_pk_mul_f32 v[248:249], v[0:1], v[90:91] op_sel_hi:[0,1]
	v_pk_mul_f32 v[250:251], v[0:1], v[94:95] op_sel_hi:[0,1]
	ds_write_b128 v238, v[248:251] offset:96
	v_pk_mul_f32 v[248:249], v[0:1], v[92:93] op_sel_hi:[0,1]
	v_pk_mul_f32 v[250:251], v[0:1], v[108:109] op_sel_hi:[0,1]
	ds_write_b128 v238, v[248:251] offset:128
	v_pk_mul_f32 v[248:249], v[0:1], v[110:111] op_sel_hi:[0,1]
	v_pk_mul_f32 v[250:251], v[0:1], v[176:177] op_sel_hi:[0,1]
	ds_write_b128 v238, v[248:251] offset:160
	v_pk_mul_f32 v[248:249], v[0:1], v[174:175] op_sel_hi:[0,1]
	v_pk_mul_f32 v[250:251], v[0:1], v[192:193] op_sel_hi:[0,1]
	ds_write_b128 v238, v[248:251] offset:192
	v_pk_mul_f32 v[248:249], v[0:1], v[194:195] op_sel_hi:[0,1]
	v_pk_mul_f32 v[250:251], v[0:1], v[206:207] op_sel_hi:[0,1]
	ds_write_b128 v238, v[248:251] offset:224
	v_add_u32_e32 v252, 0x100, v253
	v_and_or_b32 v2, v252, s54, v1
	ds_read_b128 v[248:251], v246
	ds_read_b128 v[160:163], v246 offset:1088
	s_waitcnt lgkmcnt(1)
	global_store_dwordx4 v2, v[248:251], s[10:11] sc0 nt
	s_nop 0
	ds_read_b128 v[248:251], v246 offset:2176
	v_or_b32_e32 v3, 0x8000, v2
	s_waitcnt lgkmcnt(1)
	global_store_dwordx4 v3, v[160:163], s[10:11] sc0 nt
	s_nop 0
	ds_read_b128 v[160:163], v246 offset:3264
	v_or_b32_e32 v252, 0x10000, v2
	s_waitcnt lgkmcnt(1)
	global_store_dwordx4 v252, v[248:251], s[10:11] sc0 nt
	s_nop 0
	ds_read_b128 v[248:251], v246 offset:4352
	v_or_b32_e32 v3, 0x18000, v2
	s_waitcnt lgkmcnt(1)
	global_store_dwordx4 v3, v[160:163], s[10:11] sc0 nt
	s_nop 0
	ds_read_b128 v[160:163], v246 offset:5440
	v_or_b32_e32 v252, 0x20000, v2
	s_waitcnt lgkmcnt(1)
	global_store_dwordx4 v252, v[248:251], s[10:11] sc0 nt
	s_nop 0
	ds_read_b128 v[248:251], v246 offset:6528
	v_or_b32_e32 v3, 0x28000, v2
	s_waitcnt lgkmcnt(1)
	global_store_dwordx4 v3, v[160:163], s[10:11] sc0 nt
	s_nop 0
	ds_read_b128 v[160:163], v246 offset:7616
	v_or_b32_e32 v252, 0x30000, v2
	s_waitcnt lgkmcnt(1)
	global_store_dwordx4 v252, v[248:251], s[10:11] sc0 nt
	v_or_b32_e32 v3, 0x38000, v2
	s_waitcnt lgkmcnt(0)
	global_store_dwordx4 v3, v[160:163], s[10:11] sc0 nt
	s_cmp_eq_u32 s12, 28
	s_cbranch_scc1 .Lkl_skip
	s_add_i32 s63, s62, 0x3000
	s_and_b32 s63, s63, 0x3f000
	s_or_b32 s63, s63, s58
	v_or_b32_e32 v2, s63, v231
	global_load_dwordx4 v[80:83], v2, s[6:7]
	global_load_dwordx4 v[84:87], v2, s[6:7] offset:1024
	global_load_dwordx4 v[88:91], v2, s[6:7] offset:2048
	global_load_dwordx4 v[92:95], v2, s[6:7] offset:3072
	s_add_i32 s63, s62, 0x2000
	s_and_b32 s63, s63, 0x3f000
	s_or_b32 s63, s63, s58
	v_or_b32_e32 v3, s63, v231
	global_load_dwordx4 v[96:99], v3, s[6:7]
	global_load_dwordx4 v[100:103], v3, s[6:7] offset:1024
	global_load_dwordx4 v[108:111], v3, s[6:7] offset:2048
	global_load_dwordx4 v[192:195], v3, s[6:7] offset:3072
	s_add_i32 s63, s62, 0x1000
	s_and_b32 s63, s63, 0x3f000
	s_or_b32 s63, s63, s58
	v_or_b32_e32 v2, s63, v231
	global_load_dwordx4 v[174:177], v2, s[6:7] offset:2048
	global_load_dwordx4 v[178:181], v2, s[6:7] offset:3072
.Lkl_skip:
	v_pk_mul_f32 v[248:249], v[0:1], v[64:65] op_sel_hi:[0,1]
	v_pk_mul_f32 v[250:251], v[0:1], v[66:67] op_sel_hi:[0,1]
	ds_write_b128 v238, v[248:251]
	v_pk_mul_f32 v[248:249], v[0:1], v[68:69] op_sel_hi:[0,1]
	v_pk_mul_f32 v[250:251], v[0:1], v[74:75] op_sel_hi:[0,1]
	ds_write_b128 v238, v[248:251] offset:32
	v_pk_mul_f32 v[248:249], v[0:1], v[72:73] op_sel_hi:[0,1]
	v_pk_mul_f32 v[250:251], v[0:1], v[104:105] op_sel_hi:[0,1]
	ds_write_b128 v238, v[248:251] offset:64
	v_pk_mul_f32 v[248:249], v[0:1], v[106:107] op_sel_hi:[0,1]
	v_pk_mul_f32 v[250:251], v[0:1], v[172:173] op_sel_hi:[0,1]
	ds_write_b128 v238, v[248:251] offset:96
	v_pk_mul_f32 v[248:249], v[0:1], v[170:171] op_sel_hi:[0,1]
	v_pk_mul_f32 v[250:251], v[0:1], v[188:189] op_sel_hi:[0,1]
	ds_write_b128 v238, v[248:251] offset:128
	v_pk_mul_f32 v[248:249], v[0:1], v[190:191] op_sel_hi:[0,1]
	v_pk_mul_f32 v[250:251], v[0:1], v[202:203] op_sel_hi:[0,1]
	ds_write_b128 v238, v[248:251] offset:160
	v_pk_mul_f32 v[248:249], v[0:1], v[200:201] op_sel_hi:[0,1]
	v_pk_mul_f32 v[250:251], v[0:1], v[214:215] op_sel_hi:[0,1]
	ds_write_b128 v238, v[248:251] offset:192
	v_pk_mul_f32 v[248:249], v[0:1], v[216:217] op_sel_hi:[0,1]
	v_pk_mul_f32 v[250:251], v[0:1], v[222:223] op_sel_hi:[0,1]
	ds_write_b128 v238, v[248:251] offset:224
	v_add_u32_e32 v252, 0x200, v253
	v_and_or_b32 v2, v252, s54, v1
	ds_read_b128 v[248:251], v246
	ds_read_b128 v[160:163], v246 offset:1088
	s_waitcnt lgkmcnt(1)
	global_store_dwordx4 v2, v[248:251], s[10:11] sc0 nt
	s_nop 0
	ds_read_b128 v[248:251], v246 offset:2176
	v_or_b32_e32 v3, 0x8000, v2
	s_waitcnt lgkmcnt(1)
	global_store_dwordx4 v3, v[160:163], s[10:11] sc0 nt
	s_nop 0
	ds_read_b128 v[160:163], v246 offset:3264
	v_or_b32_e32 v252, 0x10000, v2
	s_waitcnt lgkmcnt(1)
	global_store_dwordx4 v252, v[248:251], s[10:11] sc0 nt
	s_nop 0
	ds_read_b128 v[248:251], v246 offset:4352
	v_or_b32_e32 v3, 0x18000, v2
	s_waitcnt lgkmcnt(1)
	global_store_dwordx4 v3, v[160:163], s[10:11] sc0 nt
	s_nop 0
	ds_read_b128 v[160:163], v246 offset:5440
	v_or_b32_e32 v252, 0x20000, v2
	s_waitcnt lgkmcnt(1)
	global_store_dwordx4 v252, v[248:251], s[10:11] sc0 nt
	s_nop 0
	ds_read_b128 v[248:251], v246 offset:6528
	v_or_b32_e32 v3, 0x28000, v2
	s_waitcnt lgkmcnt(1)
	global_store_dwordx4 v3, v[160:163], s[10:11] sc0 nt
	s_nop 0
	ds_read_b128 v[160:163], v246 offset:7616
	v_or_b32_e32 v252, 0x30000, v2
	s_waitcnt lgkmcnt(1)
	global_store_dwordx4 v252, v[248:251], s[10:11] sc0 nt
	v_or_b32_e32 v3, 0x38000, v2
	s_waitcnt lgkmcnt(0)
	global_store_dwordx4 v3, v[160:163], s[10:11] sc0 nt
	v_pk_mul_f32 v[248:249], v[0:1], v[70:71] op_sel_hi:[0,1]
	v_pk_mul_f32 v[250:251], v[0:1], v[76:77] op_sel_hi:[0,1]
	ds_write_b128 v238, v[248:251]
	v_pk_mul_f32 v[248:249], v[0:1], v[78:79] op_sel_hi:[0,1]
	v_pk_mul_f32 v[250:251], v[0:1], v[168:169] op_sel_hi:[0,1]
	ds_write_b128 v238, v[248:251] offset:32
	v_pk_mul_f32 v[248:249], v[0:1], v[126:127] op_sel_hi:[0,1]
	v_pk_mul_f32 v[250:251], v[0:1], v[184:185] op_sel_hi:[0,1]
	ds_write_b128 v238, v[248:251] offset:64
	v_pk_mul_f32 v[248:249], v[0:1], v[186:187] op_sel_hi:[0,1]
	v_pk_mul_f32 v[250:251], v[0:1], v[198:199] op_sel_hi:[0,1]
	ds_write_b128 v238, v[248:251] offset:96
	v_pk_mul_f32 v[248:249], v[0:1], v[196:197] op_sel_hi:[0,1]
	v_pk_mul_f32 v[250:251], v[0:1], v[210:211] op_sel_hi:[0,1]
	ds_write_b128 v238, v[248:251] offset:128
	v_pk_mul_f32 v[248:249], v[0:1], v[212:213] op_sel_hi:[0,1]
	v_pk_mul_f32 v[250:251], v[0:1], v[220:221] op_sel_hi:[0,1]
	ds_write_b128 v238, v[248:251] offset:160
	v_pk_mul_f32 v[248:249], v[0:1], v[218:219] op_sel_hi:[0,1]
	v_pk_mul_f32 v[250:251], v[0:1], v[224:225] op_sel_hi:[0,1]
	ds_write_b128 v238, v[248:251] offset:192
	v_pk_mul_f32 v[248:249], v[0:1], v[226:227] op_sel_hi:[0,1]
	v_pk_mul_f32 v[250:251], v[0:1], v[228:229] op_sel_hi:[0,1]
	ds_write_b128 v238, v[248:251] offset:224
	v_add_u32_e32 v252, 0x300, v253
	v_and_or_b32 v2, v252, s54, v1
	ds_read_b128 v[248:251], v246
	ds_read_b128 v[160:163], v246 offset:1088
	s_waitcnt lgkmcnt(1)
	global_store_dwordx4 v2, v[248:251], s[10:11] sc0 nt
	s_nop 0
	ds_read_b128 v[248:251], v246 offset:2176
	v_or_b32_e32 v3, 0x8000, v2
	s_waitcnt lgkmcnt(1)
	global_store_dwordx4 v3, v[160:163], s[10:11] sc0 nt
	s_nop 0
	ds_read_b128 v[160:163], v246 offset:3264
	v_or_b32_e32 v252, 0x10000, v2
	s_waitcnt lgkmcnt(1)
	global_store_dwordx4 v252, v[248:251], s[10:11] sc0 nt
	s_nop 0
	ds_read_b128 v[248:251], v246 offset:4352
	v_or_b32_e32 v3, 0x18000, v2
	s_waitcnt lgkmcnt(1)
	global_store_dwordx4 v3, v[160:163], s[10:11] sc0 nt
	s_nop 0
	ds_read_b128 v[160:163], v246 offset:5440
	v_or_b32_e32 v252, 0x20000, v2
	s_waitcnt lgkmcnt(1)
	global_store_dwordx4 v252, v[248:251], s[10:11] sc0 nt
	s_nop 0
	ds_read_b128 v[248:251], v246 offset:6528
	v_or_b32_e32 v3, 0x28000, v2
	s_waitcnt lgkmcnt(1)
	global_store_dwordx4 v3, v[160:163], s[10:11] sc0 nt
	s_nop 0
	ds_read_b128 v[160:163], v246 offset:7616
	v_or_b32_e32 v252, 0x30000, v2
	s_waitcnt lgkmcnt(1)
	global_store_dwordx4 v252, v[248:251], s[10:11] sc0 nt
	v_or_b32_e32 v3, 0x38000, v2
	s_waitcnt lgkmcnt(0)
	global_store_dwordx4 v3, v[160:163], s[10:11] sc0 nt
	s_mov_b32 s57, s24
	s_add_i32 s12, s12, 4
	s_cmp_eq_u32 s12, 32
	s_cbranch_scc1 .LBB1_22
